# s12 + x1 prologue de-serialisation: bulk loads issued before the wait on the first gate load; the forget-gate scan runs under them (counted vmcnt waits)
# speedup vs baseline: 1.0086x; 1.0086x over previous
; __device__ __forceinline__ void x1_wave(int item, int b0, const h16* __restrict__ proj, const float* __restrict__ small, const float* __restrict__ convw, ...
;     int lane = threadIdx.x & 63; (void)lane_in; asm volatile("" : "+v"(lane));
;     const int r32 = lane & 31, hi = lane >> 5;
;     const int c = item & 31, hh = (item >> 5) & 3, bl = item >> 7;
;     const size_t row0 = (size_t)bl * SEQ + c * 64;
;     const int gbh = (b0 + bl) * 4 + hh, lbh = bl * 4 + hh;
;     const int dg = lane & 15, rq = lane >> 4, isk = dg >> 3, pcol = isk ? 256 + hh * 64 + (dg - 8) * 8 : hh * 64 + dg * 8;
;     const float* sp = small + ((size_t)b0 * SEQ + row0 + lane) * 16;
;     const float li = sp[8 + hh], lf = sp[12 + hh];
;     const h16* vp = proj + row0 * PP + PC_CV + hh * 128 + (size_t)(lane >> 2) * PP + (lane & 3) * 8;
;     h16x8 xv[4][4];
; #pragma unroll
;     for (int sg = 0; sg < 4; ++sg)
; #pragma unroll
;         for (int vb = 0; vb < 4; ++vb) xv[sg][vb] = *(const h16x8*)(vp + (size_t)(16 * sg) * PP + 32 * vb);
;     h16x8 xin[19];
;     {   const int tl0 = c * 64 + rq * 16 - 3;
;         const h16* xp = proj + (size_t)bl * SEQ * PP + PC_CQK + pcol;
; #pragma unroll
;         for (int r = 0; r < 19; ++r) { const int tt = tl0 + r; xin[r] = *(const h16x8*)(xp + (size_t)(tt < 0 ? 0 : tt) * PP); }
;     }
;     f32x4 wq[4][2];
; #pragma unroll
;     for (int j = 0; j < 4; ++j) { wq[j][0] = *(const f32x4*)(convw + j * 512 + pcol); wq[j][1] = *(const f32x4*)(convw + j * 512 + pcol + 4); }
.LBB0_882:
	s_ashr_i32 s20, s6, 7
	s_add_i32 s0, s20, s4
	v_mov_b32_e32 v174, v250
	s_bfe_u32 s13, s6, 0x20005
	s_lshl_b32 s0, s0, 2
	s_waitcnt lgkmcnt(0)
	s_and_b32 s12, s6, 31
	s_ashr_i32 s21, s20, 31
	s_or_b32 s14, s0, s13
	v_and_b32_e32 v178, 15, v174
	s_lshl_b32 s0, s13, 6
	s_lshl_b64 s[40:41], s[20:21], 11
	s_lshl_b32 s15, s12, 6
	v_lshlrev_b32_e32 v0, 3, v178
	s_add_i32 s1, s0, 0xc0
	s_or_b32 s40, s40, s15
	v_add_u32_e32 v1, s1, v0
	v_or_b32_e32 v0, s0, v0
	v_readlane_b32 s0, v255, 43
	s_add_u32 s0, s40, s0
	v_cmp_gt_u32_e32 vcc, 8, v178
	s_addc_u32 s1, s41, 0
	v_ashrrev_i32_e32 v175, 31, v174
	v_cndmask_b32_e32 v42, v1, v0, vcc
	v_lshl_add_u64 v[0:1], s[0:1], 0, v[174:175]
	v_lshlrev_b64 v[0:1], 6, v[0:1]
	v_lshl_add_u64 v[0:1], s[86:87], 0, v[0:1]
	s_lshl_b32 s28, s13, 2
	v_lshl_add_u64 v[0:1], v[0:1], 0, s[28:29]
	global_load_dword v194, v[0:1], off offset:48
	s_mul_i32 s0, s41, 0x3800
	s_mul_hi_u32 s1, s40, 0x3800
	s_add_i32 s1, s1, s0
	s_mul_i32 s0, s40, 0x3800
	s_add_u32 s0, s16, s0
	s_addc_u32 s1, s17, s1
	s_lshl_b32 s18, s13, 8
	s_add_u32 s0, s0, s18
	s_addc_u32 s1, s1, 0
	s_add_u32 s0, s0, 0x2400
	s_addc_u32 s1, s1, 0
	v_ashrrev_i32_e32 v4, 2, v174
	v_mov_b64_e32 v[2:3], s[0:1]
	v_mad_i64_i32 v[2:3], s[0:1], v4, s91, v[2:3]
	v_lshlrev_b32_e32 v4, 3, v174
	v_and_b32_e32 v179, 24, v4
	v_lshlrev_b32_e32 v96, 1, v179
	v_lshl_add_u64 v[4:5], v[2:3], 0, v[96:97]
	global_load_dwordx4 v[84:87], v[4:5], off
	global_load_dword v190, v[0:1], off offset:32
	global_load_dwordx4 v[98:101], v[4:5], off offset:64
	global_load_dwordx4 v[102:105], v[4:5], off offset:128
	v_add_co_u32_e64 v0, s[0:1], s96, v4
	v_lshlrev_b32_e32 v191, 2, v174
	s_nop 0
	v_addc_co_u32_e64 v1, s[0:1], 0, v5, s[0:1]
	s_mov_b32 s0, 0x70000
	s_nop 0
	v_add_co_u32_e64 v2, s[0:1], s0, v4
	global_load_dwordx4 v[106:109], v[4:5], off offset:192
	global_load_dwordx4 v[110:113], v[0:1], off
	v_addc_co_u32_e64 v3, s[0:1], 0, v5, s[0:1]
	s_mov_b32 s0, 0xa8000
	s_nop 0
	v_add_co_u32_e64 v4, s[0:1], s0, v4
	v_and_b32_e32 v176, -16, v174
	s_nop 0
	v_addc_co_u32_e64 v5, s[0:1], 0, v5, s[0:1]
	s_mul_i32 s0, s20, 0x1c00000
	v_add_u32_e32 v193, -4, v191
	s_mul_hi_i32 s1, s20, 0x1c00000
	s_add_u32 s0, s16, s0
	v_add_u32_e32 v14, s15, v176
	s_addc_u32 s1, s17, s1
	v_lshlrev_b32_e32 v96, 1, v42
	v_add_u32_e32 v43, -3, v14
	v_lshl_add_u64 v[6:7], s[0:1], 0, v[96:97]
	s_mov_b64 s[0:1], 0x2000
	v_max_i32_e32 v10, -1, v43
	v_add_u32_e32 v12, -1, v14
	v_max_i32_e32 v16, -4, v43
	v_max_i32_e32 v18, -5, v43
	v_max_i32_e32 v20, -6, v43
	v_max_i32_e32 v22, -7, v43
	v_max_i32_e32 v24, -8, v43
	v_lshl_add_u64 v[6:7], v[6:7], 0, s[0:1]
	v_max_i32_e32 v8, 0, v43
	v_add_u32_e32 v10, 1, v10
	v_max_i32_e32 v12, 0, v12
	v_max_i32_e32 v14, 0, v14
	v_add_u32_e32 v16, 4, v16
	v_add_u32_e32 v18, 5, v18
	v_add_u32_e32 v20, 6, v20
	v_add_u32_e32 v22, 7, v22
	v_add_u32_e32 v24, 8, v24
	v_mad_u64_u32 v[8:9], s[0:1], v8, s91, v[6:7]
	v_mad_u64_u32 v[10:11], s[0:1], v10, s91, v[6:7]
	v_mad_u64_u32 v[12:13], s[0:1], v12, s91, v[6:7]
	v_mad_u64_u32 v[14:15], s[0:1], v14, s91, v[6:7]
	v_mad_u64_u32 v[16:17], s[0:1], v16, s91, v[6:7]
	v_mad_u64_u32 v[18:19], s[0:1], v18, s91, v[6:7]
	v_mad_u64_u32 v[20:21], s[0:1], v20, s91, v[6:7]
	v_mad_u64_u32 v[22:23], s[0:1], v22, s91, v[6:7]
	v_max_i32_e32 v26, -9, v43
	v_add_u32_e32 v26, 9, v26
	v_mad_u64_u32 v[24:25], s[0:1], v24, s91, v[6:7]
	v_mad_u64_u32 v[26:27], s[0:1], v26, s91, v[6:7]
	v_max_i32_e32 v34, -13, v43
	v_max_i32_e32 v36, -14, v43
	v_max_i32_e32 v28, -10, v43
	v_add_u32_e32 v28, 10, v28
	v_mad_u64_u32 v[28:29], s[0:1], v28, s91, v[6:7]
	v_max_i32_e32 v38, -15, v43
	v_max_i32_e32 v40, -16, v43
	v_max_i32_e32 v30, -11, v43
	v_add_u32_e32 v30, 11, v30
	v_mad_u64_u32 v[30:31], s[0:1], v30, s91, v[6:7]
	v_max_i32_e32 v44, 0xffffffef, v43
	v_add_u32_e32 v34, 13, v34
	v_max_i32_e32 v32, -12, v43
	v_max_i32_e32 v43, 0xffffffee, v43
	v_add_u32_e32 v32, 12, v32
	v_add_u32_e32 v36, 14, v36
	v_add_u32_e32 v38, 15, v38
	v_add_u32_e32 v40, 16, v40
	v_add_u32_e32 v44, 17, v44
	v_add_u32_e32 v43, 18, v43
	v_mad_u64_u32 v[32:33], s[0:1], v32, s91, v[6:7]
	v_mad_u64_u32 v[34:35], s[0:1], v34, s91, v[6:7]
	v_mad_u64_u32 v[36:37], s[0:1], v36, s91, v[6:7]
	v_mad_u64_u32 v[38:39], s[0:1], v38, s91, v[6:7]
	v_mad_u64_u32 v[40:41], s[0:1], v40, s91, v[6:7]
	v_mad_u64_u32 v[180:181], s[0:1], v44, s91, v[6:7]
	v_mad_u64_u32 v[6:7], s[0:1], v43, s91, v[6:7]
	v_lshlrev_b32_e32 v182, 2, v42
	v_mov_b32_e32 v183, v97
	v_lshl_add_u64 v[42:43], s[2:3], 0, v[182:183]
	s_mov_b64 s[0:1], 0x1000
	v_lshl_add_u64 v[184:185], v[42:43], 0, s[0:1]
	s_movk_i32 s0, 0x1000
	v_add_co_u32_e64 v186, s[0:1], s0, v42
	v_cmp_lt_u32_e64 s[38:39], 7, v178
	s_nop 0
	v_addc_co_u32_e64 v187, s[0:1], 0, v43, s[0:1]
	s_mov_b64 s[0:1], 0x1800
	s_nop 0
	v_lshl_add_u64 v[188:189], v[42:43], 0, s[0:1]
	global_load_dwordx4 v[130:133], v[0:1], off offset:64
	global_load_dwordx4 v[134:137], v[0:1], off offset:128
	global_load_dwordx4 v[138:141], v[0:1], off offset:192
	global_load_dwordx4 v[142:145], v[2:3], off
	global_load_dwordx4 v[146:149], v[2:3], off offset:64
	global_load_dwordx4 v[150:153], v[2:3], off offset:128
	global_load_dwordx4 v[154:157], v[2:3], off offset:192
	global_load_dwordx4 v[158:161], v[4:5], off
	global_load_dwordx4 v[162:165], v[4:5], off offset:64
	global_load_dwordx4 v[166:169], v[4:5], off offset:128
	global_load_dwordx4 v[170:173], v[4:5], off offset:192
	global_load_dwordx4 v[126:129], v[8:9], off
	global_load_dwordx4 v[122:125], v[10:11], off
	global_load_dwordx4 v[118:121], v[12:13], off
	global_load_dwordx4 v[114:117], v[14:15], off
	global_load_dwordx4 v[92:95], v[16:17], off
	global_load_dwordx4 v[88:91], v[18:19], off
	global_load_dwordx4 v[80:83], v[20:21], off
	global_load_dwordx4 v[76:79], v[22:23], off
	global_load_dwordx4 v[72:75], v[24:25], off
	global_load_dwordx4 v[68:71], v[26:27], off
	global_load_dwordx4 v[64:67], v[28:29], off
	global_load_dwordx4 v[60:63], v[30:31], off
	global_load_dwordx4 v[56:59], v[32:33], off
	global_load_dwordx4 v[52:55], v[34:35], off
	global_load_dwordx4 v[48:51], v[36:37], off
	global_load_dwordx4 v[44:47], v[38:39], off
	s_nop 0
	global_load_dwordx4 v[40:43], v[40:41], off
	s_nop 0
	global_load_dwordx4 v[36:39], v[180:181], off
	s_nop 0
	global_load_dwordx4 v[4:7], v[6:7], off
	s_nop 0
	global_load_dwordx4 v[8:11], v182, s[2:3] offset:16
	global_load_dwordx4 v[24:27], v182, s[2:3]
	global_load_dwordx4 v[12:15], v182, s[2:3] offset:2064
	global_load_dwordx4 v[28:31], v182, s[2:3] offset:2048
	global_load_dwordx4 v[16:19], v[184:185], off offset:16
	global_load_dwordx4 v[32:35], v[186:187], off
	global_load_dwordx4 v[20:23], v[186:187], off offset:2048
	global_load_dwordx4 v[0:3], v[188:189], off offset:16
	s_waitcnt vmcnt(44)
; __device__ __forceinline__ float shfl_idx(float x, int srclane) { return __int_as_float(__builtin_amdgcn_ds_bpermute(srclane << 2, __float_as_int(x))); }
; #define LFW(off) ((__attribute__((address_space(3))) float*)(R + W_SC + (off)))
; __device__ __forceinline__ void x1_wave(int item, int b0, const h16* __restrict__ proj, const float* __restrict__ small, const float* __restrict__ convw, ...
;     ...
;     {   float bc = lf;
; #pragma unroll
;         for (int o = 1; o < 64; o <<= 1) { const float u = shfl_idx(bc, lane - o); if (lane >= o) bc += u; }
;         const float as = li - bc; float mx = as;
; #pragma unroll
;         for (int o = 1; o < 64; o <<= 1) mx = fmaxf(mx, shfl_idx(mx, lane ^ o));
;         LFW(0)[lane] = __expf(as - mx);
;         if (lane == 63) { amax[gbh * 32 + c] = mx; blast[gbh * 32 + c] = bc; } }
	ds_bpermute_b32 v195, v193, v194
	s_waitcnt lgkmcnt(0)
	v_add_f32_e32 v195, v194, v195
	v_cmp_gt_i32_e64 s[0:1], 1, v174
	s_nop 1
	v_cndmask_b32_e64 v196, v195, v194, s[0:1]
	v_add_u32_e32 v193, -8, v191
	ds_bpermute_b32 v197, v193, v196
	s_waitcnt lgkmcnt(0)
	v_add_f32_e32 v197, v196, v197
	v_cmp_gt_i32_e64 s[0:1], 2, v174
	s_nop 1
	v_cndmask_b32_e64 v198, v197, v196, s[0:1]
	v_add_u32_e32 v193, -16, v191
	ds_bpermute_b32 v199, v193, v198
	s_waitcnt lgkmcnt(0)
	v_add_f32_e32 v199, v198, v199
	v_cmp_gt_i32_e64 s[0:1], 4, v174
	s_nop 1
	v_cndmask_b32_e64 v177, v199, v198, s[0:1]
	v_subrev_u32_e32 v193, 32, v191
	ds_bpermute_b32 v192, v193, v177
	s_waitcnt lgkmcnt(0)
	v_add_f32_e32 v180, v177, v192
	v_cmp_gt_i32_e64 s[0:1], 8, v174
	v_xor_b32_e32 v182, 8, v191
	s_nop 0
	v_cndmask_b32_e64 v177, v180, v177, s[0:1]
	v_subrev_u32_e32 v180, 64, v191
	ds_bpermute_b32 v180, v180, v177
	v_cmp_gt_i32_e64 s[0:1], 16, v174
	s_waitcnt lgkmcnt(0)
	v_add_f32_e32 v180, v177, v180
	v_cndmask_b32_e64 v180, v180, v177, s[0:1]
	v_add_u32_e32 v177, 0xffffff80, v191
	ds_bpermute_b32 v177, v177, v180
	v_cmp_gt_i32_e64 s[0:1], 32, v174
	s_waitcnt lgkmcnt(0)
	v_add_f32_e32 v177, v180, v177
	v_cndmask_b32_e64 v180, v177, v180, s[0:1]
	s_waitcnt vmcnt(38)
	v_sub_f32_e32 v181, v190, v180
	v_xor_b32_e32 v180, 4, v191
	ds_bpermute_b32 v180, v180, v181
	v_cmp_eq_u32_e64 s[0:1], 63, v174
	s_waitcnt lgkmcnt(0)
	v_max_f32_e32 v180, v180, v180
	v_max_f32_e32 v180, v181, v180
	ds_bpermute_b32 v182, v182, v180
	s_waitcnt lgkmcnt(0)
	v_max_f32_e32 v182, v182, v182
	v_max_f32_e32 v180, v180, v182
	v_xor_b32_e32 v182, 16, v191
	ds_bpermute_b32 v182, v182, v180
	s_waitcnt lgkmcnt(0)
	v_max_f32_e32 v182, v182, v182
	v_max_f32_e32 v180, v180, v182
	v_xor_b32_e32 v182, 32, v191
	ds_bpermute_b32 v182, v182, v180
	s_waitcnt lgkmcnt(0)
	v_max_f32_e32 v182, v182, v182
	v_max_f32_e32 v180, v180, v182
	v_xor_b32_e32 v182, 64, v191
	ds_bpermute_b32 v182, v182, v180
	s_waitcnt lgkmcnt(0)
	v_max_f32_e32 v182, v182, v182
	v_max_f32_e32 v180, v180, v182
	v_xor_b32_e32 v182, 0x80, v191
	ds_bpermute_b32 v182, v182, v180
	s_waitcnt lgkmcnt(0)
	v_max_f32_e32 v182, v182, v182
	v_max_f32_e32 v180, v180, v182
	v_sub_f32_e32 v181, v181, v180
	v_mul_f32_e32 v181, 0x3fb8aa3b, v181
	v_exp_f32_e32 v181, v181
	v_add_u32_e32 v182, s10, v191
	ds_write_b32 v182, v181 offset:25088
	s_and_saveexec_b64 s[42:43], s[0:1]
	s_cbranch_execz .LBB0_884
	s_lshl_b32 s0, s14, 5
	s_or_b32 s0, s0, s12
	s_ashr_i32 s1, s0, 31
	s_lshl_b64 s[0:1], s[0:1], 2
	v_readlane_b32 s18, v254, 34
	v_readlane_b32 s19, v254, 35
	s_add_u32 s18, s18, s0
	s_addc_u32 s19, s19, s1
	v_readlane_b32 s26, v254, 32
	v_readlane_b32 s27, v254, 33
	s_add_u32 s0, s26, s0
	s_addc_u32 s1, s27, s1
	s_movk_i32 s27, 0x2000
	global_store_dword v97, v180, s[18:19]
	global_store_dword v97, v177, s[0:1]
